# v18 + MFMA/LDS interleave: first 16 P.V V-fragment tr reads of each tile issued right after the last QK lgkmcnt wait (before softmax-finish cvt block), diff + MLA loops
# baseline (speedup 1.0000x reference)
; template <int I, int N, class F> __device__ __forceinline__ void sfor(F&& f) { if constexpr (I < N) { f(std::integral_constant<int, I>{}); sfor<I + 1, N>(f); } }
; template <int N> __device__ __forceinline__ void lgkm_wait8(s16x4* v) { asm volatile("s_waitcnt lgkmcnt(%8)" : "+v"(v[0]), "+v"(v[1]), "+v"(v[2]), "+v"(v[3]), "+v"(v[4]), "+v"(v[5]), "+v"(v[6]), "+v"(v[7]) : "n"(N) : "memory"); }
; __device__ __forceinline__ void finishSM(f32x16& p0, f32x16& p1, float& l_reg, bf16x8& pa0, bf16x8& pa1, bf16x8& pa2, bf16x8& pa3) {
; #pragma unroll
;   for (int r = 0; r < 16; ++r) p1[r] = __builtin_amdgcn_exp2f(p1[r]);
;   float ps = 0;
; #pragma unroll
;   for (int r = 0; r < 16; ++r) ps += p0[r];
; #pragma unroll
;   for (int r = 0; r < 16; ++r) ps += p1[r];
;   l_reg += ps;
;     ...
;   ATT_PK4(p0, 0, pa0); ATT_PK4(p0, 8, pa1); ATT_PK4(p1, 0, pa2); ATT_PK4(p1, 8, pa3);
;     ...
; }
; template <int DV, int GRP> __device__ __forceinline__ void v_group_read(s16x4* vf, int vb) {
;   sfor<0, 8>([&](auto ic) { constexpr int j = decltype(ic)::value; vf[j] = tr_read<v_rd_off<DV>(GRP, j / 2, j % 2)>(vb); });
; }
; __device__ __forceinline__ void pv_group(f32x16& od, const s16x4* vf, bf16x8 pa0, bf16x8 pa1, bf16x8 pa2, bf16x8 pa3) {
;     ...
;   od = __builtin_amdgcn_mfma_f32_32x32x16_bf16(pa0, ATT_PK(vf[0], vf[1]), od, 0, 0, 0);
;   od = __builtin_amdgcn_mfma_f32_32x32x16_bf16(pa1, ATT_PK(vf[2], vf[3]), od, 0, 0, 0);
;   od = __builtin_amdgcn_mfma_f32_32x32x16_bf16(pa2, ATT_PK(vf[4], vf[5]), od, 0, 0, 0);
;   od = __builtin_amdgcn_mfma_f32_32x32x16_bf16(pa3, ATT_PK(vf[6], vf[7]), od, 0, 0, 0);
;     ...
; }
; template <int DV> __device__ __forceinline__ void pv_all_pipe(f32x16* o, int vb, bf16x8 pa0, bf16x8 pa1, bf16x8 pa2, bf16x8 pa3) {
;   s16x4 va[8], vc[8];
;   v_group_read<DV, 0>(va, vb); v_group_read<DV, 1>(vc, vb);
;   lgkm_wait8<8>(va); pv_group(o[0], va, pa0, pa1, pa2, pa3);
;   if constexpr (DV == 128) {
;     s16x4 vd[8], ve[8];
;     v_group_read<DV, 2>(vd, vb);
;     lgkm_wait8<8>(vc); pv_group(o[1], vc, pa0, pa1, pa2, pa3);
;     v_group_read<DV, 3>(ve, vb);
;     lgkm_wait8<8>(vd); pv_group(o[2], vd, pa0, pa1, pa2, pa3);
;     lgkm_wait8<0>(ve); pv_group(o[3], ve, pa0, pa1, pa2, pa3);
;   } else { lgkm_wait8<0>(vc); pv_group(o[1], vc, pa0, pa1, pa2, pa3); }
; }
.Lstg_c1_done:
	ds_read_b128 v[130:133], v166 offset:16384
	ds_read_b128 v[134:137], v166 offset:20480
	v_add_f32_e32 v180, v66, v180
	v_add_f32_e32 v180, v67, v180
	v_add_f32_e32 v180, v68, v180
	v_add_f32_e32 v180, v69, v180
	v_add_f32_e32 v180, v70, v180
	v_add_f32_e32 v180, v71, v180
	v_add_f32_e32 v180, v72, v180
	v_add_f32_e32 v180, v73, v180
	s_waitcnt lgkmcnt(0)
	v_mfma_f32_32x32x16_bf16 v[98:113], v[130:133], v[122:125], v[98:113]
	v_mfma_f32_32x32x16_bf16 v[82:97], v[134:137], v[122:125], v[82:97]
	ds_read_b128 v[130:133], v168 offset:16384
	ds_read_b128 v[134:137], v168 offset:20480
	v_add_f32_e32 v180, v74, v180
	v_add_f32_e32 v180, v75, v180
	v_add_f32_e32 v180, v76, v180
	v_add_f32_e32 v180, v77, v180
	v_add_f32_e32 v180, v78, v180
	v_add_f32_e32 v180, v79, v180
	v_add_f32_e32 v180, v80, v180
	v_add_f32_e32 v180, v81, v180
	s_waitcnt lgkmcnt(0)
	ds_read_b64_tr_b16 v[176:177], v169 offset:0
	ds_read_b64_tr_b16 v[178:179], v169 offset:0x800
	ds_read_b64_tr_b16 v[198:199], v169 offset:0x1000
	ds_read_b64_tr_b16 v[200:201], v169 offset:0x1800
	ds_read_b64_tr_b16 v[202:203], v169 offset:0x2000
	ds_read_b64_tr_b16 v[204:205], v169 offset:0x2800
	ds_read_b64_tr_b16 v[206:207], v169 offset:0x3000
	ds_read_b64_tr_b16 v[208:209], v169 offset:0x3800
	ds_read_b64_tr_b16 v[210:211], v169 offset:0x200
	ds_read_b64_tr_b16 v[212:213], v169 offset:0xa00
	ds_read_b64_tr_b16 v[214:215], v169 offset:0x1200
	ds_read_b64_tr_b16 v[216:217], v169 offset:0x1a00
	ds_read_b64_tr_b16 v[218:219], v169 offset:0x2200
	ds_read_b64_tr_b16 v[220:221], v169 offset:0x2a00
	ds_read_b64_tr_b16 v[222:223], v169 offset:0x3200
	ds_read_b64_tr_b16 v[224:225], v169 offset:0x3a00
	v_mfma_f32_32x32x16_bf16 v[98:113], v[130:133], v[126:129], v[98:113]
	v_mfma_f32_32x32x16_bf16 v[82:97], v[134:137], v[126:129], v[82:97]
	v_add_f32_e32 v172, v172, v180
	v_cvt_pk_bf16_f32 v130, v173, v174
	v_cvt_pk_bf16_f32 v131, v175, v184
	v_cvt_pk_bf16_f32 v132, v185, v186
	v_cvt_pk_bf16_f32 v133, v187, v188
	v_cvt_pk_bf16_f32 v134, v189, v190
	v_cvt_pk_bf16_f32 v135, v191, v192
	v_cvt_pk_bf16_f32 v136, v193, v194
	v_cvt_pk_bf16_f32 v137, v195, v196
	v_cvt_pk_bf16_f32 v138, v66, v67
	v_cvt_pk_bf16_f32 v139, v68, v69
	v_cvt_pk_bf16_f32 v140, v70, v71
	v_cvt_pk_bf16_f32 v141, v72, v73
	v_cvt_pk_bf16_f32 v142, v74, v75
	v_cvt_pk_bf16_f32 v143, v76, v77
	v_cvt_pk_bf16_f32 v144, v78, v79
	v_cvt_pk_bf16_f32 v145, v80, v81
	s_nop 0
	v_permlane32_swap_b32_e32 v130, v132
	v_permlane32_swap_b32_e32 v131, v133
	s_waitcnt lgkmcnt(8)
	v_permlane32_swap_b32_e32 v134, v136
	s_nop 0
	v_mfma_f32_32x32x16_bf16 v[2:17], v[130:133], v[176:179], v[2:17]
	v_permlane32_swap_b32_e32 v135, v137
	v_permlane32_swap_b32_e32 v138, v140
	v_permlane32_swap_b32_e32 v139, v141
	ds_read_b64_tr_b16 v[176:177], v169 offset:0x400
	v_mfma_f32_32x32x16_bf16 v[2:17], v[134:137], v[198:201], v[2:17]
	v_permlane32_swap_b32_e32 v142, v144
	v_permlane32_swap_b32_e32 v143, v145
	ds_read_b64_tr_b16 v[178:179], v169 offset:0xc00
	ds_read_b64_tr_b16 v[198:199], v169 offset:0x1400
	ds_read_b64_tr_b16 v[200:201], v169 offset:0x1c00
	v_mfma_f32_32x32x16_bf16 v[2:17], v[138:141], v[202:205], v[2:17]
	ds_read_b64_tr_b16 v[202:203], v169 offset:0x2400
	ds_read_b64_tr_b16 v[204:205], v169 offset:0x2c00
	v_exp_f32_e32 v197, v98
	v_mfma_f32_32x32x16_bf16 v[2:17], v[142:145], v[206:209], v[2:17]
	ds_read_b64_tr_b16 v[206:207], v169 offset:0x3400
	ds_read_b64_tr_b16 v[208:209], v169 offset:0x3c00
	s_waitcnt lgkmcnt(8)
	s_nop 0
	v_mfma_f32_32x32x16_bf16 v[50:65], v[130:133], v[210:213], v[50:65]
	ds_read_b64_tr_b16 v[210:211], v169 offset:0x600
	ds_read_b64_tr_b16 v[212:213], v169 offset:0xe00
	v_mfma_f32_32x32x16_bf16 v[50:65], v[134:137], v[214:217], v[50:65]
	ds_read_b64_tr_b16 v[214:215], v169 offset:0x1600
	ds_read_b64_tr_b16 v[216:217], v169 offset:0x1e00
	v_mfma_f32_32x32x16_bf16 v[50:65], v[138:141], v[218:221], v[50:65]
	ds_read_b64_tr_b16 v[218:219], v169 offset:0x2600
	ds_read_b64_tr_b16 v[220:221], v169 offset:0x2e00
	v_mfma_f32_32x32x16_bf16 v[50:65], v[142:145], v[222:225], v[50:65]
	ds_read_b64_tr_b16 v[222:223], v169 offset:0x3600
	ds_read_b64_tr_b16 v[224:225], v169 offset:0x3e00
	s_waitcnt lgkmcnt(8)
	s_nop 0
	s_waitcnt lgkmcnt(0)
	v_mfma_f32_32x32x16_bf16 v[34:49], v[130:133], v[176:179], v[34:49]
	v_mfma_f32_32x32x16_bf16 v[18:33], v[130:133], v[210:213], v[18:33]
	v_exp_f32_e32 v210, v105
	v_exp_f32_e32 v211, v111
	v_exp_f32_e32 v212, v113
	v_mfma_f32_32x32x16_bf16 v[34:49], v[134:137], v[198:201], v[34:49]
	v_exp_f32_e32 v200, v99
	v_exp_f32_e32 v198, v100
	v_exp_f32_e32 v199, v106
	v_exp_f32_e32 v201, v108
	v_mfma_f32_32x32x16_bf16 v[18:33], v[134:137], v[214:217], v[18:33]
	v_mfma_f32_32x32x16_bf16 v[34:49], v[138:141], v[202:205], v[34:49]
	v_exp_f32_e32 v202, v101
	v_exp_f32_e32 v204, v102
	v_exp_f32_e32 v205, v104
	v_exp_f32_e32 v203, v107
	v_mfma_f32_32x32x16_bf16 v[18:33], v[138:141], v[218:221], v[18:33]
	v_mfma_f32_32x32x16_bf16 v[34:49], v[142:145], v[206:209], v[34:49]
	v_exp_f32_e32 v207, v103
	v_exp_f32_e32 v209, v109
	v_exp_f32_e32 v206, v110
	v_exp_f32_e32 v208, v112
	v_mfma_f32_32x32x16_bf16 v[18:33], v[142:145], v[222:225], v[18:33]
	s_cbranch_vccnz .LBB0_865

; template <int N> __device__ __forceinline__ void lgkm_wait8(s16x4* v) { asm volatile("s_waitcnt lgkmcnt(%8)" : "+v"(v[0]), "+v"(v[1]), "+v"(v[2]), "+v"(v[3]), "+v"(v[4]), "+v"(v[5]), "+v"(v[6]), "+v"(v[7]) : "n"(N) : "memory"); }
; __device__ __forceinline__ void finishSM(f32x16& p0, f32x16& p1, float& l_reg, bf16x8& pa0, bf16x8& pa1, bf16x8& pa2, bf16x8& pa3) {
; #pragma unroll
;   for (int r = 0; r < 16; ++r) p1[r] = __builtin_amdgcn_exp2f(p1[r]);
;   float ps = 0;
; #pragma unroll
;   for (int r = 0; r < 16; ++r) ps += p0[r];
; #pragma unroll
;   for (int r = 0; r < 16; ++r) ps += p1[r];
;   l_reg += ps;
;     ...
;   ATT_PK4(p0, 0, pa0); ATT_PK4(p0, 8, pa1); ATT_PK4(p1, 0, pa2); ATT_PK4(p1, 8, pa3);
;     ...
; }
; template <int DK>
; __device__ __forceinline__ void qkt(f32x16& p0, f32x16& p1, const char* Ks, const bf16x8* qr, int r32, int hi) {
;   p0 = f32x16{}; p1 = f32x16{};
; #pragma unroll
;   for (int d0 = 0; d0 < DK / 16; ++d0) { const int cb = (d0 * 16 + hi * 8) * 2;
;     const bf16x8 b0 = *reinterpret_cast<const bf16x8*>(Ks + ATT_KSWZ(r32, cb));
;     const bf16x8 b1 = *reinterpret_cast<const bf16x8*>(Ks + ATT_KSWZ(32 + r32, cb));
;     p0 = __builtin_amdgcn_mfma_f32_32x32x16_bf16(b0, qr[d0], p0, 0, 0, 0);
;     p1 = __builtin_amdgcn_mfma_f32_32x32x16_bf16(b1, qr[d0], p1, 0, 0, 0);
;   }
; template <int DV> __device__ __forceinline__ void pv_all_pipe(f32x16* o, int vb, bf16x8 pa0, bf16x8 pa1, bf16x8 pa2, bf16x8 pa3) {
;   s16x4 va[8], vc[8];
;   v_group_read<DV, 0>(va, vb); v_group_read<DV, 1>(vc, vb);
;   lgkm_wait8<8>(va); pv_group(o[0], va, pa0, pa1, pa2, pa3);
;   if constexpr (DV == 128) {
;     s16x4 vd[8], ve[8];
;     v_group_read<DV, 2>(vd, vb);
;     lgkm_wait8<8>(vc); pv_group(o[1], vc, pa0, pa1, pa2, pa3);
;     v_group_read<DV, 3>(ve, vb);
;     lgkm_wait8<8>(vd); pv_group(o[2], vd, pa0, pa1, pa2, pa3);
;     lgkm_wait8<0>(ve); pv_group(o[3], ve, pa0, pa1, pa2, pa3);
;   } else { lgkm_wait8<0>(vc); pv_group(o[1], vc, pa0, pa1, pa2, pa3); }
.Lstg_l2:
	v_exp_f32_e32 v90, v90
	v_exp_f32_e32 v91, v91
	v_exp_f32_e32 v92, v92
	v_exp_f32_e32 v93, v93
	v_exp_f32_e32 v94, v94
	v_exp_f32_e32 v95, v95
	v_exp_f32_e32 v96, v96
	v_mfma_f32_32x32x16_bf16 v[98:113], v[130:133], v[118:121], v[98:113]
	v_exp_f32_e32 v97, v97
	v_mfma_f32_32x32x16_bf16 v[66:81], v[134:137], v[118:121], v[66:81]
	ds_read_b128 v[130:133], v166 offset:32768
	ds_read_b128 v[134:137], v166 offset:36864
	v_add_f32_e32 v180, v82, v180
	v_add_f32_e32 v180, v83, v180
	v_add_f32_e32 v180, v84, v180
	v_add_f32_e32 v180, v85, v180
	v_add_f32_e32 v180, v86, v180
	v_add_f32_e32 v180, v87, v180
	v_add_f32_e32 v180, v88, v180
	v_add_f32_e32 v180, v89, v180
	s_waitcnt lgkmcnt(0)
	v_mfma_f32_32x32x16_bf16 v[98:113], v[130:133], v[122:125], v[98:113]
	v_mfma_f32_32x32x16_bf16 v[66:81], v[134:137], v[122:125], v[66:81]
	ds_read_b128 v[130:133], v168 offset:32768
	ds_read_b128 v[134:137], v168 offset:36864
	v_add_f32_e32 v180, v90, v180
	v_add_f32_e32 v180, v91, v180
	v_add_f32_e32 v180, v92, v180
	v_add_f32_e32 v180, v93, v180
	v_add_f32_e32 v180, v94, v180
	v_add_f32_e32 v180, v95, v180
	v_add_f32_e32 v180, v96, v180
	v_add_f32_e32 v180, v97, v180
	s_waitcnt lgkmcnt(0)
	ds_read_b64_tr_b16 v[174:175], v170 offset:0
	ds_read_b64_tr_b16 v[176:177], v170 offset:0x800
	ds_read_b64_tr_b16 v[184:185], v170 offset:0x1000
	ds_read_b64_tr_b16 v[186:187], v170 offset:0x1800
	ds_read_b64_tr_b16 v[188:189], v170 offset:0x2000
	ds_read_b64_tr_b16 v[190:191], v170 offset:0x2800
	ds_read_b64_tr_b16 v[192:193], v170 offset:0x3000
	ds_read_b64_tr_b16 v[194:195], v170 offset:0x3800
	ds_read_b64_tr_b16 v[214:215], v170 offset:0x200
	ds_read_b64_tr_b16 v[216:217], v170 offset:0xa00
	ds_read_b64_tr_b16 v[218:219], v170 offset:0x1200
	ds_read_b64_tr_b16 v[220:221], v170 offset:0x1a00
	ds_read_b64_tr_b16 v[222:223], v170 offset:0x2200
	ds_read_b64_tr_b16 v[224:225], v170 offset:0x2a00
	ds_read_b64_tr_b16 v[226:227], v170 offset:0x3200
	ds_read_b64_tr_b16 v[228:229], v170 offset:0x3a00
	v_mfma_f32_32x32x16_bf16 v[98:113], v[130:133], v[126:129], v[98:113]
	v_mfma_f32_32x32x16_bf16 v[66:81], v[134:137], v[126:129], v[66:81]
	v_add_f32_e32 v172, v172, v180
	v_cvt_pk_bf16_f32 v130, v197, v200
	v_cvt_pk_bf16_f32 v131, v198, v202
	v_cvt_pk_bf16_f32 v132, v204, v207
	v_cvt_pk_bf16_f32 v133, v205, v210
	v_cvt_pk_bf16_f32 v134, v199, v203
	v_cvt_pk_bf16_f32 v135, v201, v209
	v_cvt_pk_bf16_f32 v136, v206, v211
	v_cvt_pk_bf16_f32 v137, v208, v212
	v_cvt_pk_bf16_f32 v138, v82, v83
	v_cvt_pk_bf16_f32 v139, v84, v85
	v_cvt_pk_bf16_f32 v140, v86, v87
	v_cvt_pk_bf16_f32 v141, v88, v89
	v_cvt_pk_bf16_f32 v142, v90, v91
	v_cvt_pk_bf16_f32 v143, v92, v93
	v_cvt_pk_bf16_f32 v144, v94, v95
	v_cvt_pk_bf16_f32 v145, v96, v97
	s_nop 0
	v_permlane32_swap_b32_e32 v130, v132
	v_permlane32_swap_b32_e32 v131, v133
	s_waitcnt lgkmcnt(8)
	v_permlane32_swap_b32_e32 v134, v136
	s_nop 0
	v_mfma_f32_32x32x16_bf16 v[2:17], v[130:133], v[174:177], v[2:17]
	v_permlane32_swap_b32_e32 v135, v137
	v_permlane32_swap_b32_e32 v138, v140
	v_permlane32_swap_b32_e32 v139, v141
	ds_read_b64_tr_b16 v[174:175], v170 offset:0x400
	v_mfma_f32_32x32x16_bf16 v[2:17], v[134:137], v[184:187], v[2:17]
	v_permlane32_swap_b32_e32 v142, v144
	v_permlane32_swap_b32_e32 v143, v145
	ds_read_b64_tr_b16 v[176:177], v170 offset:0xc00
	ds_read_b64_tr_b16 v[184:185], v170 offset:0x1400
	ds_read_b64_tr_b16 v[186:187], v170 offset:0x1c00
	v_mfma_f32_32x32x16_bf16 v[2:17], v[138:141], v[188:191], v[2:17]
	ds_read_b64_tr_b16 v[188:189], v170 offset:0x2400
	ds_read_b64_tr_b16 v[190:191], v170 offset:0x2c00
	v_exp_f32_e32 v173, v98
	v_exp_f32_e32 v196, v113
	v_mfma_f32_32x32x16_bf16 v[2:17], v[142:145], v[192:195], v[2:17]
	ds_read_b64_tr_b16 v[192:193], v170 offset:0x3400
	ds_read_b64_tr_b16 v[194:195], v170 offset:0x3c00
	s_waitcnt lgkmcnt(8)
	s_nop 0
	v_mfma_f32_32x32x16_bf16 v[50:65], v[130:133], v[214:217], v[50:65]
	ds_read_b64_tr_b16 v[214:215], v170 offset:0x600
	ds_read_b64_tr_b16 v[216:217], v170 offset:0xe00
	v_mfma_f32_32x32x16_bf16 v[50:65], v[134:137], v[218:221], v[50:65]
	ds_read_b64_tr_b16 v[218:219], v170 offset:0x1600
	ds_read_b64_tr_b16 v[220:221], v170 offset:0x1e00
	v_mfma_f32_32x32x16_bf16 v[50:65], v[138:141], v[222:225], v[50:65]
	ds_read_b64_tr_b16 v[222:223], v170 offset:0x2600
	ds_read_b64_tr_b16 v[224:225], v170 offset:0x2e00
	v_mfma_f32_32x32x16_bf16 v[50:65], v[142:145], v[226:229], v[50:65]
	ds_read_b64_tr_b16 v[226:227], v170 offset:0x3600
	ds_read_b64_tr_b16 v[228:229], v170 offset:0x3e00
	s_waitcnt lgkmcnt(8)
	s_nop 0
	s_waitcnt lgkmcnt(0)
	v_mfma_f32_32x32x16_bf16 v[34:49], v[130:133], v[174:177], v[34:49]
	v_exp_f32_e32 v174, v99
	v_exp_f32_e32 v175, v100
	v_mfma_f32_32x32x16_bf16 v[18:33], v[130:133], v[214:217], v[18:33]
	v_mfma_f32_32x32x16_bf16 v[34:49], v[134:137], v[184:187], v[34:49]
	v_exp_f32_e32 v184, v101
	v_exp_f32_e32 v185, v102
	v_exp_f32_e32 v186, v103
	v_exp_f32_e32 v187, v104
	v_mfma_f32_32x32x16_bf16 v[18:33], v[134:137], v[218:221], v[18:33]
	v_mfma_f32_32x32x16_bf16 v[34:49], v[138:141], v[188:191], v[34:49]
	v_exp_f32_e32 v188, v105
	v_exp_f32_e32 v189, v106
	v_exp_f32_e32 v190, v107
	v_exp_f32_e32 v191, v108
	v_mfma_f32_32x32x16_bf16 v[18:33], v[138:141], v[222:225], v[18:33]
	v_mfma_f32_32x32x16_bf16 v[34:49], v[142:145], v[192:195], v[34:49]
	v_exp_f32_e32 v192, v109
	v_exp_f32_e32 v193, v110
	v_exp_f32_e32 v194, v111
	v_exp_f32_e32 v195, v112
	v_mfma_f32_32x32x16_bf16 v[18:33], v[142:145], v[226:229], v[18:33]
	s_andn2_b64 vcc, exec, s[24:25]
	s_cbranch_vccz .LBB0_866

; template <int N> __device__ __forceinline__ void lgkm_wait8(s16x4* v) { asm volatile("s_waitcnt lgkmcnt(%8)" : "+v"(v[0]), "+v"(v[1]), "+v"(v[2]), "+v"(v[3]), "+v"(v[4]), "+v"(v[5]), "+v"(v[6]), "+v"(v[7]) : "n"(N) : "memory"); }
; __device__ __forceinline__ void finishSM(f32x16& p0, f32x16& p1, float& l_reg, bf16x8& pa0, bf16x8& pa1, bf16x8& pa2, bf16x8& pa3) {
; #pragma unroll
;   for (int r = 0; r < 16; ++r) p1[r] = __builtin_amdgcn_exp2f(p1[r]);
;   float ps = 0;
; #pragma unroll
;   for (int r = 0; r < 16; ++r) ps += p0[r];
; #pragma unroll
;   for (int r = 0; r < 16; ++r) ps += p1[r];
;   l_reg += ps;
;     ...
;   ATT_PK4(p0, 0, pa0); ATT_PK4(p0, 8, pa1); ATT_PK4(p1, 0, pa2); ATT_PK4(p1, 8, pa3);
;     ...
; }
; template <int DK>
; __device__ __forceinline__ void qkt(f32x16& p0, f32x16& p1, const char* Ks, const bf16x8* qr, int r32, int hi) {
;   p0 = f32x16{}; p1 = f32x16{};
; #pragma unroll
;   for (int d0 = 0; d0 < DK / 16; ++d0) { const int cb = (d0 * 16 + hi * 8) * 2;
;     const bf16x8 b0 = *reinterpret_cast<const bf16x8*>(Ks + ATT_KSWZ(r32, cb));
;     const bf16x8 b1 = *reinterpret_cast<const bf16x8*>(Ks + ATT_KSWZ(32 + r32, cb));
;     p0 = __builtin_amdgcn_mfma_f32_32x32x16_bf16(b0, qr[d0], p0, 0, 0, 0);
;     p1 = __builtin_amdgcn_mfma_f32_32x32x16_bf16(b1, qr[d0], p1, 0, 0, 0);
;   }
; template <int DV> __device__ __forceinline__ void pv_all_pipe(f32x16* o, int vb, bf16x8 pa0, bf16x8 pa1, bf16x8 pa2, bf16x8 pa3) {
;   s16x4 va[8], vc[8];
;   v_group_read<DV, 0>(va, vb); v_group_read<DV, 1>(vc, vb);
;   lgkm_wait8<8>(va); pv_group(o[0], va, pa0, pa1, pa2, pa3);
;   if constexpr (DV == 128) {
;     s16x4 vd[8], ve[8];
;     v_group_read<DV, 2>(vd, vb);
;     lgkm_wait8<8>(vc); pv_group(o[1], vc, pa0, pa1, pa2, pa3);
;     v_group_read<DV, 3>(ve, vb);
;     lgkm_wait8<8>(vd); pv_group(o[2], vd, pa0, pa1, pa2, pa3);
;     lgkm_wait8<0>(ve); pv_group(o[3], ve, pa0, pa1, pa2, pa3);
;   } else { lgkm_wait8<0>(vc); pv_group(o[1], vc, pa0, pa1, pa2, pa3); }
.Lstg_l3:
	v_exp_f32_e32 v74, v74
	v_exp_f32_e32 v75, v75
	v_exp_f32_e32 v76, v76
	v_exp_f32_e32 v77, v77
	v_exp_f32_e32 v78, v78
	v_exp_f32_e32 v79, v79
	v_exp_f32_e32 v80, v80
	v_mfma_f32_32x32x16_bf16 v[98:113], v[130:133], v[118:121], v[98:113]
	v_exp_f32_e32 v81, v81
	v_mfma_f32_32x32x16_bf16 v[82:97], v[134:137], v[118:121], v[82:97]
	ds_read_b128 v[130:133], v166 offset:49152
	ds_read_b128 v[134:137], v166 offset:53248
	v_add_f32_e32 v180, v66, v180
	v_add_f32_e32 v180, v67, v180
	v_add_f32_e32 v180, v68, v180
	v_add_f32_e32 v180, v69, v180
	v_add_f32_e32 v180, v70, v180
	v_add_f32_e32 v180, v71, v180
	v_add_f32_e32 v180, v72, v180
	v_add_f32_e32 v180, v73, v180
	s_waitcnt lgkmcnt(0)
	v_mfma_f32_32x32x16_bf16 v[98:113], v[130:133], v[122:125], v[98:113]
	v_mfma_f32_32x32x16_bf16 v[82:97], v[134:137], v[122:125], v[82:97]
	ds_read_b128 v[130:133], v168 offset:49152
	ds_read_b128 v[134:137], v168 offset:53248
	v_add_f32_e32 v180, v74, v180
	v_add_f32_e32 v180, v75, v180
	v_add_f32_e32 v180, v76, v180
	v_add_f32_e32 v180, v77, v180
	v_add_f32_e32 v180, v78, v180
	v_add_f32_e32 v180, v79, v180
	v_add_f32_e32 v180, v80, v180
	v_add_f32_e32 v180, v81, v180
	s_waitcnt lgkmcnt(0)
	ds_read_b64_tr_b16 v[176:177], v171 offset:0
	ds_read_b64_tr_b16 v[178:179], v171 offset:0x800
	ds_read_b64_tr_b16 v[198:199], v171 offset:0x1000
	ds_read_b64_tr_b16 v[200:201], v171 offset:0x1800
	ds_read_b64_tr_b16 v[202:203], v171 offset:0x2000
	ds_read_b64_tr_b16 v[204:205], v171 offset:0x2800
	ds_read_b64_tr_b16 v[206:207], v171 offset:0x3000
	ds_read_b64_tr_b16 v[208:209], v171 offset:0x3800
	ds_read_b64_tr_b16 v[210:211], v171 offset:0x200
	ds_read_b64_tr_b16 v[212:213], v171 offset:0xa00
	ds_read_b64_tr_b16 v[214:215], v171 offset:0x1200
	ds_read_b64_tr_b16 v[216:217], v171 offset:0x1a00
	ds_read_b64_tr_b16 v[218:219], v171 offset:0x2200
	ds_read_b64_tr_b16 v[220:221], v171 offset:0x2a00
	ds_read_b64_tr_b16 v[222:223], v171 offset:0x3200
	ds_read_b64_tr_b16 v[224:225], v171 offset:0x3a00
	v_mfma_f32_32x32x16_bf16 v[98:113], v[130:133], v[126:129], v[98:113]
	v_mfma_f32_32x32x16_bf16 v[82:97], v[134:137], v[126:129], v[82:97]
	v_add_f32_e32 v172, v172, v180
	v_cvt_pk_bf16_f32 v130, v173, v174
	v_cvt_pk_bf16_f32 v131, v175, v184
	v_cvt_pk_bf16_f32 v132, v185, v186
	v_cvt_pk_bf16_f32 v133, v187, v188
	v_cvt_pk_bf16_f32 v134, v189, v190
	v_cvt_pk_bf16_f32 v135, v191, v192
	v_cvt_pk_bf16_f32 v136, v193, v194
	v_cvt_pk_bf16_f32 v137, v195, v196
	v_cvt_pk_bf16_f32 v138, v66, v67
	v_cvt_pk_bf16_f32 v139, v68, v69
	v_cvt_pk_bf16_f32 v140, v70, v71
	v_cvt_pk_bf16_f32 v141, v72, v73
	v_cvt_pk_bf16_f32 v142, v74, v75
	v_cvt_pk_bf16_f32 v143, v76, v77
	v_cvt_pk_bf16_f32 v144, v78, v79
	v_cvt_pk_bf16_f32 v145, v80, v81
	s_nop 0
	v_permlane32_swap_b32_e32 v130, v132
	v_permlane32_swap_b32_e32 v131, v133
	s_waitcnt lgkmcnt(8)
	v_permlane32_swap_b32_e32 v134, v136
	s_nop 0
	v_mfma_f32_32x32x16_bf16 v[2:17], v[130:133], v[176:179], v[2:17]
	v_permlane32_swap_b32_e32 v135, v137
	v_permlane32_swap_b32_e32 v138, v140
	v_permlane32_swap_b32_e32 v139, v141
	ds_read_b64_tr_b16 v[176:177], v171 offset:0x400
	v_mfma_f32_32x32x16_bf16 v[2:17], v[134:137], v[198:201], v[2:17]
	v_permlane32_swap_b32_e32 v142, v144
	v_permlane32_swap_b32_e32 v143, v145
	ds_read_b64_tr_b16 v[178:179], v171 offset:0xc00
	ds_read_b64_tr_b16 v[198:199], v171 offset:0x1400
	ds_read_b64_tr_b16 v[200:201], v171 offset:0x1c00
	v_mfma_f32_32x32x16_bf16 v[2:17], v[138:141], v[202:205], v[2:17]
	ds_read_b64_tr_b16 v[202:203], v171 offset:0x2400
	ds_read_b64_tr_b16 v[204:205], v171 offset:0x2c00
	v_exp_f32_e32 v197, v98
	v_mfma_f32_32x32x16_bf16 v[2:17], v[142:145], v[206:209], v[2:17]
	ds_read_b64_tr_b16 v[206:207], v171 offset:0x3400
	ds_read_b64_tr_b16 v[208:209], v171 offset:0x3c00
	s_waitcnt lgkmcnt(8)
	s_nop 0
	v_mfma_f32_32x32x16_bf16 v[50:65], v[130:133], v[210:213], v[50:65]
	ds_read_b64_tr_b16 v[210:211], v171 offset:0x600
	ds_read_b64_tr_b16 v[212:213], v171 offset:0xe00
	v_mfma_f32_32x32x16_bf16 v[50:65], v[134:137], v[214:217], v[50:65]
	ds_read_b64_tr_b16 v[214:215], v171 offset:0x1600
	ds_read_b64_tr_b16 v[216:217], v171 offset:0x1e00
	v_mfma_f32_32x32x16_bf16 v[50:65], v[138:141], v[218:221], v[50:65]
	ds_read_b64_tr_b16 v[218:219], v171 offset:0x2600
	ds_read_b64_tr_b16 v[220:221], v171 offset:0x2e00
	v_mfma_f32_32x32x16_bf16 v[50:65], v[142:145], v[222:225], v[50:65]
	ds_read_b64_tr_b16 v[222:223], v171 offset:0x3600
	ds_read_b64_tr_b16 v[224:225], v171 offset:0x3e00
	s_waitcnt lgkmcnt(8)
	s_nop 0
	s_waitcnt lgkmcnt(0)
	v_mfma_f32_32x32x16_bf16 v[34:49], v[130:133], v[176:179], v[34:49]
	v_mfma_f32_32x32x16_bf16 v[18:33], v[130:133], v[210:213], v[18:33]
	v_exp_f32_e32 v210, v105
	v_exp_f32_e32 v211, v111
	v_exp_f32_e32 v212, v113
	v_mfma_f32_32x32x16_bf16 v[34:49], v[134:137], v[198:201], v[34:49]
	v_exp_f32_e32 v200, v99
	v_exp_f32_e32 v198, v100
	v_exp_f32_e32 v199, v106
	v_exp_f32_e32 v201, v108
	v_mfma_f32_32x32x16_bf16 v[18:33], v[134:137], v[214:217], v[18:33]
	v_mfma_f32_32x32x16_bf16 v[34:49], v[138:141], v[202:205], v[34:49]
	v_exp_f32_e32 v202, v101
	v_exp_f32_e32 v204, v102
	v_exp_f32_e32 v205, v104
	v_exp_f32_e32 v203, v107
	v_mfma_f32_32x32x16_bf16 v[18:33], v[138:141], v[218:221], v[18:33]
	v_mfma_f32_32x32x16_bf16 v[34:49], v[142:145], v[206:209], v[34:49]
	v_exp_f32_e32 v207, v103
	v_exp_f32_e32 v209, v109
	v_exp_f32_e32 v206, v110
	v_exp_f32_e32 v208, v112
	v_mfma_f32_32x32x16_bf16 v[18:33], v[142:145], v[222:225], v[18:33]
	s_cmp_ge_u32 s57, s97
	s_cbranch_scc1 .LBB0_880

; template <int N> __device__ __forceinline__ void lgkm_wait8(s16x4* v) { asm volatile("s_waitcnt lgkmcnt(%8)" : "+v"(v[0]), "+v"(v[1]), "+v"(v[2]), "+v"(v[3]), "+v"(v[4]), "+v"(v[5]), "+v"(v[6]), "+v"(v[7]) : "n"(N) : "memory"); }
; __device__ __forceinline__ void finishSM(f32x16& p0, f32x16& p1, float& l_reg, bf16x8& pa0, bf16x8& pa1, bf16x8& pa2, bf16x8& pa3) {
; #pragma unroll
;   for (int r = 0; r < 16; ++r) p1[r] = __builtin_amdgcn_exp2f(p1[r]);
;   float ps = 0;
; #pragma unroll
;   for (int r = 0; r < 16; ++r) ps += p0[r];
; #pragma unroll
;   for (int r = 0; r < 16; ++r) ps += p1[r];
;   l_reg += ps;
;     ...
;   ATT_PK4(p0, 0, pa0); ATT_PK4(p0, 8, pa1); ATT_PK4(p1, 0, pa2); ATT_PK4(p1, 8, pa3);
;     ...
; }
; template <int DK>
; __device__ __forceinline__ void qkt(f32x16& p0, f32x16& p1, const char* Ks, const bf16x8* qr, int r32, int hi) {
;   p0 = f32x16{}; p1 = f32x16{};
; #pragma unroll
;   for (int d0 = 0; d0 < DK / 16; ++d0) { const int cb = (d0 * 16 + hi * 8) * 2;
;     const bf16x8 b0 = *reinterpret_cast<const bf16x8*>(Ks + ATT_KSWZ(r32, cb));
;     const bf16x8 b1 = *reinterpret_cast<const bf16x8*>(Ks + ATT_KSWZ(32 + r32, cb));
;     p0 = __builtin_amdgcn_mfma_f32_32x32x16_bf16(b0, qr[d0], p0, 0, 0, 0);
;     p1 = __builtin_amdgcn_mfma_f32_32x32x16_bf16(b1, qr[d0], p1, 0, 0, 0);
;   }
; template <int DV> __device__ __forceinline__ void pv_all_pipe(f32x16* o, int vb, bf16x8 pa0, bf16x8 pa1, bf16x8 pa2, bf16x8 pa3) {
;   s16x4 va[8], vc[8];
;   v_group_read<DV, 0>(va, vb); v_group_read<DV, 1>(vc, vb);
;   lgkm_wait8<8>(va); pv_group(o[0], va, pa0, pa1, pa2, pa3);
;   if constexpr (DV == 128) {
;     s16x4 vd[8], ve[8];
;     v_group_read<DV, 2>(vd, vb);
;     lgkm_wait8<8>(vc); pv_group(o[1], vc, pa0, pa1, pa2, pa3);
;     v_group_read<DV, 3>(ve, vb);
;     lgkm_wait8<8>(vd); pv_group(o[2], vd, pa0, pa1, pa2, pa3);
;     lgkm_wait8<0>(ve); pv_group(o[3], ve, pa0, pa1, pa2, pa3);
;   } else { lgkm_wait8<0>(vc); pv_group(o[1], vc, pa0, pa1, pa2, pa3); }
.Lstg_l4:
	v_exp_f32_e32 v91, v91
	v_exp_f32_e32 v92, v92
	v_exp_f32_e32 v93, v93
	v_exp_f32_e32 v94, v94
	v_exp_f32_e32 v95, v95
	v_exp_f32_e32 v96, v96
	v_exp_f32_e32 v97, v97
	v_mfma_f32_32x32x16_bf16 v[98:113], v[130:133], v[118:121], v[98:113]
	v_mfma_f32_32x32x16_bf16 v[66:81], v[134:137], v[118:121], v[66:81]
	ds_read_b128 v[130:133], v166
	ds_read_b128 v[134:137], v166 offset:4096
	v_add_f32_e32 v180, v82, v180
	v_add_f32_e32 v180, v83, v180
	v_add_f32_e32 v180, v84, v180
	v_add_f32_e32 v180, v85, v180
	v_add_f32_e32 v180, v86, v180
	v_add_f32_e32 v180, v87, v180
	v_add_f32_e32 v180, v88, v180
	v_add_f32_e32 v180, v89, v180
	s_waitcnt lgkmcnt(0)
	v_mfma_f32_32x32x16_bf16 v[98:113], v[130:133], v[122:125], v[98:113]
	v_mfma_f32_32x32x16_bf16 v[66:81], v[134:137], v[122:125], v[66:81]
	ds_read_b128 v[130:133], v168
	ds_read_b128 v[134:137], v168 offset:4096
	v_add_f32_e32 v180, v90, v180
	v_add_f32_e32 v180, v91, v180
	v_add_f32_e32 v180, v92, v180
	v_add_f32_e32 v180, v93, v180
	v_add_f32_e32 v180, v94, v180
	v_add_f32_e32 v180, v95, v180
	v_add_f32_e32 v180, v96, v180
	v_add_f32_e32 v180, v97, v180
	s_waitcnt lgkmcnt(0)
	ds_read_b64_tr_b16 v[174:175], v160 offset:0
	ds_read_b64_tr_b16 v[176:177], v160 offset:0x800
	ds_read_b64_tr_b16 v[184:185], v160 offset:0x1000
	ds_read_b64_tr_b16 v[186:187], v160 offset:0x1800
	ds_read_b64_tr_b16 v[188:189], v160 offset:0x2000
	ds_read_b64_tr_b16 v[190:191], v160 offset:0x2800
	ds_read_b64_tr_b16 v[192:193], v160 offset:0x3000
	ds_read_b64_tr_b16 v[194:195], v160 offset:0x3800
	ds_read_b64_tr_b16 v[214:215], v160 offset:0x200
	ds_read_b64_tr_b16 v[216:217], v160 offset:0xa00
	ds_read_b64_tr_b16 v[218:219], v160 offset:0x1200
	ds_read_b64_tr_b16 v[220:221], v160 offset:0x1a00
	ds_read_b64_tr_b16 v[222:223], v160 offset:0x2200
	ds_read_b64_tr_b16 v[224:225], v160 offset:0x2a00
	ds_read_b64_tr_b16 v[226:227], v160 offset:0x3200
	ds_read_b64_tr_b16 v[228:229], v160 offset:0x3a00
	v_mfma_f32_32x32x16_bf16 v[98:113], v[130:133], v[126:129], v[98:113]
	v_mfma_f32_32x32x16_bf16 v[66:81], v[134:137], v[126:129], v[66:81]
	v_add_f32_e32 v172, v172, v180
	v_cvt_pk_bf16_f32 v130, v197, v200
	v_cvt_pk_bf16_f32 v131, v198, v202
	v_cvt_pk_bf16_f32 v132, v204, v207
	v_cvt_pk_bf16_f32 v133, v205, v210
	v_cvt_pk_bf16_f32 v134, v199, v203
	v_cvt_pk_bf16_f32 v135, v201, v209
	v_cvt_pk_bf16_f32 v136, v206, v211
	v_cvt_pk_bf16_f32 v137, v208, v212
	v_cvt_pk_bf16_f32 v138, v82, v83
	v_cvt_pk_bf16_f32 v139, v84, v85
	v_cvt_pk_bf16_f32 v140, v86, v87
	v_cvt_pk_bf16_f32 v141, v88, v89
	v_cvt_pk_bf16_f32 v142, v90, v91
	v_cvt_pk_bf16_f32 v143, v92, v93
	v_cvt_pk_bf16_f32 v144, v94, v95
	v_cvt_pk_bf16_f32 v145, v96, v97
	s_nop 0
	v_permlane32_swap_b32_e32 v130, v132
	v_permlane32_swap_b32_e32 v131, v133
	s_waitcnt lgkmcnt(8)
	v_permlane32_swap_b32_e32 v134, v136
	s_nop 0
	v_mfma_f32_32x32x16_bf16 v[2:17], v[130:133], v[174:177], v[2:17]
	v_permlane32_swap_b32_e32 v135, v137
	v_permlane32_swap_b32_e32 v138, v140
	v_permlane32_swap_b32_e32 v139, v141
	ds_read_b64_tr_b16 v[174:175], v160 offset:0x400
	v_mfma_f32_32x32x16_bf16 v[2:17], v[134:137], v[184:187], v[2:17]
	v_permlane32_swap_b32_e32 v142, v144
	v_permlane32_swap_b32_e32 v143, v145
	ds_read_b64_tr_b16 v[176:177], v160 offset:0xc00
	ds_read_b64_tr_b16 v[184:185], v160 offset:0x1400
	ds_read_b64_tr_b16 v[186:187], v160 offset:0x1c00
	v_mfma_f32_32x32x16_bf16 v[2:17], v[138:141], v[188:191], v[2:17]
	ds_read_b64_tr_b16 v[188:189], v160 offset:0x2400
	ds_read_b64_tr_b16 v[190:191], v160 offset:0x2c00
	v_exp_f32_e32 v173, v98
	v_exp_f32_e32 v196, v113
	v_mfma_f32_32x32x16_bf16 v[2:17], v[142:145], v[192:195], v[2:17]
	ds_read_b64_tr_b16 v[192:193], v160 offset:0x3400
	ds_read_b64_tr_b16 v[194:195], v160 offset:0x3c00
	s_waitcnt lgkmcnt(8)
	s_nop 0
	v_mfma_f32_32x32x16_bf16 v[50:65], v[130:133], v[214:217], v[50:65]
	ds_read_b64_tr_b16 v[214:215], v160 offset:0x600
	ds_read_b64_tr_b16 v[216:217], v160 offset:0xe00
	v_mfma_f32_32x32x16_bf16 v[50:65], v[134:137], v[218:221], v[50:65]
	ds_read_b64_tr_b16 v[218:219], v160 offset:0x1600
	ds_read_b64_tr_b16 v[220:221], v160 offset:0x1e00
	v_mfma_f32_32x32x16_bf16 v[50:65], v[138:141], v[222:225], v[50:65]
	ds_read_b64_tr_b16 v[222:223], v160 offset:0x2600
	ds_read_b64_tr_b16 v[224:225], v160 offset:0x2e00
	v_mfma_f32_32x32x16_bf16 v[50:65], v[142:145], v[226:229], v[50:65]
	ds_read_b64_tr_b16 v[226:227], v160 offset:0x3600
	ds_read_b64_tr_b16 v[228:229], v160 offset:0x3e00
	s_waitcnt lgkmcnt(8)
	s_nop 0
	s_waitcnt lgkmcnt(0)
	v_mfma_f32_32x32x16_bf16 v[34:49], v[130:133], v[174:177], v[34:49]
	v_exp_f32_e32 v174, v99
	v_exp_f32_e32 v175, v100
	v_mfma_f32_32x32x16_bf16 v[18:33], v[130:133], v[214:217], v[18:33]
	v_mfma_f32_32x32x16_bf16 v[34:49], v[134:137], v[184:187], v[34:49]
	v_exp_f32_e32 v184, v101
	v_exp_f32_e32 v185, v102
	v_exp_f32_e32 v186, v103
	v_exp_f32_e32 v187, v104
	v_mfma_f32_32x32x16_bf16 v[18:33], v[134:137], v[218:221], v[18:33]
	v_mfma_f32_32x32x16_bf16 v[34:49], v[138:141], v[188:191], v[34:49]
	v_exp_f32_e32 v188, v105
	v_exp_f32_e32 v189, v106
	v_exp_f32_e32 v190, v107
	v_exp_f32_e32 v191, v108
	v_mfma_f32_32x32x16_bf16 v[18:33], v[138:141], v[222:225], v[18:33]
	v_mfma_f32_32x32x16_bf16 v[34:49], v[142:145], v[192:195], v[34:49]
	v_exp_f32_e32 v192, v109
	v_exp_f32_e32 v193, v110
	v_exp_f32_e32 v194, v111
	v_exp_f32_e32 v195, v112
	v_mfma_f32_32x32x16_bf16 v[18:33], v[142:145], v[226:229], v[18:33]

; template <int N> __device__ __forceinline__ void lgkm_wait8(s16x4* v) { asm volatile("s_waitcnt lgkmcnt(%8)" : "+v"(v[0]), "+v"(v[1]), "+v"(v[2]), "+v"(v[3]), "+v"(v[4]), "+v"(v[5]), "+v"(v[6]), "+v"(v[7]) : "n"(N) : "memory"); }
; __device__ __forceinline__ void finishSM(f32x16& p0, f32x16& p1, float& l_reg, bf16x8& pa0, bf16x8& pa1, bf16x8& pa2, bf16x8& pa3) {
; #pragma unroll
;   for (int r = 0; r < 16; ++r) p1[r] = __builtin_amdgcn_exp2f(p1[r]);
;   float ps = 0;
; #pragma unroll
;   for (int r = 0; r < 16; ++r) ps += p0[r];
; #pragma unroll
;   for (int r = 0; r < 16; ++r) ps += p1[r];
;   l_reg += ps;
;     ...
;   ATT_PK4(p0, 0, pa0); ATT_PK4(p0, 8, pa1); ATT_PK4(p1, 0, pa2); ATT_PK4(p1, 8, pa3);
;     ...
; }
; template <int DK>
; __device__ __forceinline__ void qkt(f32x16& p0, f32x16& p1, const char* Ks, const bf16x8* qr, int r32, int hi) {
;   p0 = f32x16{}; p1 = f32x16{};
; #pragma unroll
;   for (int d0 = 0; d0 < DK / 16; ++d0) { const int cb = (d0 * 16 + hi * 8) * 2;
;     const bf16x8 b0 = *reinterpret_cast<const bf16x8*>(Ks + ATT_KSWZ(r32, cb));
;     const bf16x8 b1 = *reinterpret_cast<const bf16x8*>(Ks + ATT_KSWZ(32 + r32, cb));
;     p0 = __builtin_amdgcn_mfma_f32_32x32x16_bf16(b0, qr[d0], p0, 0, 0, 0);
;     p1 = __builtin_amdgcn_mfma_f32_32x32x16_bf16(b1, qr[d0], p1, 0, 0, 0);
;   }
; template <int DV> __device__ __forceinline__ void pv_all_pipe(f32x16* o, int vb, bf16x8 pa0, bf16x8 pa1, bf16x8 pa2, bf16x8 pa3) {
;   s16x4 va[8], vc[8];
;   v_group_read<DV, 0>(va, vb); v_group_read<DV, 1>(vc, vb);
;   lgkm_wait8<8>(va); pv_group(o[0], va, pa0, pa1, pa2, pa3);
;   if constexpr (DV == 128) {
;     s16x4 vd[8], ve[8];
;     v_group_read<DV, 2>(vd, vb);
;     lgkm_wait8<8>(vc); pv_group(o[1], vc, pa0, pa1, pa2, pa3);
;     v_group_read<DV, 3>(ve, vb);
;     lgkm_wait8<8>(vd); pv_group(o[2], vd, pa0, pa1, pa2, pa3);
;     lgkm_wait8<0>(ve); pv_group(o[3], ve, pa0, pa1, pa2, pa3);
;   } else { lgkm_wait8<0>(vc); pv_group(o[1], vc, pa0, pa1, pa2, pa3); }
.Lmstag_4:
	ds_read_b128 v[82:85], v128 offset:32768
	ds_read_b128 v[86:89], v128 offset:40960
	v_add_f32_e32 v0, v194, v0
	v_add_f32_e32 v0, v188, v0
	v_add_f32_e32 v0, v191, v0
	v_add_f32_e32 v0, v190, v0
	v_add_f32_e32 v0, v196, v0
	v_add_f32_e32 v0, v195, v0
	s_waitcnt lgkmcnt(0)
	v_mfma_f32_32x32x16_bf16 v[66:81], v[82:85], v[106:109], v[66:81]
	v_add_f32_e32 v0, v198, v0
	v_add_f32_e32 v0, v197, v0
	v_add_f32_e32 v0, v199, v0
	v_add_f32_e32 v0, v34, v0
	v_add_f32_e32 v0, v35, v0
	v_add_f32_e32 v0, v36, v0
	v_add_f32_e32 v0, v37, v0
	v_mfma_f32_32x32x16_bf16 v[50:65], v[86:89], v[106:109], v[50:65]
	ds_read_b128 v[82:85], v129 offset:32768
	ds_read_b128 v[86:89], v129 offset:40960
	v_add_f32_e32 v0, v38, v0
	v_add_f32_e32 v0, v39, v0
	v_add_f32_e32 v0, v40, v0
	v_add_f32_e32 v0, v41, v0
	v_add_f32_e32 v0, v42, v0
	v_add_f32_e32 v0, v43, v0
	s_waitcnt lgkmcnt(0)
	v_mfma_f32_32x32x16_bf16 v[66:81], v[82:85], v[110:113], v[66:81]
	v_add_f32_e32 v0, v44, v0
	v_add_f32_e32 v0, v45, v0
	v_add_f32_e32 v0, v46, v0
	v_add_f32_e32 v0, v47, v0
	v_add_f32_e32 v0, v48, v0
	v_add_f32_e32 v0, v49, v0
	v_add_f32_e32 v145, v145, v0
	v_mfma_f32_32x32x16_bf16 v[50:65], v[86:89], v[110:113], v[50:65]
	ds_read_b128 v[82:85], v130 offset:32768
	ds_read_b128 v[86:89], v130 offset:40960
	s_waitcnt lgkmcnt(0)
	v_mfma_f32_32x32x16_bf16 v[66:81], v[82:85], v[114:117], v[66:81]
	v_mfma_f32_32x32x16_bf16 v[50:65], v[86:89], v[114:117], v[50:65]
	ds_read_b128 v[82:85], v131 offset:32768
	ds_read_b128 v[86:89], v131 offset:40960
	s_waitcnt lgkmcnt(0)
	ds_read_b64_tr_b16 v[154:155], v96 offset:0
	ds_read_b64_tr_b16 v[156:157], v96 offset:0x400
	ds_read_b64_tr_b16 v[158:159], v96 offset:0x800
	ds_read_b64_tr_b16 v[160:161], v96 offset:0xc00
	ds_read_b64_tr_b16 v[162:163], v96 offset:0x1000
	ds_read_b64_tr_b16 v[164:165], v96 offset:0x1400
	ds_read_b64_tr_b16 v[166:167], v96 offset:0x1800
	ds_read_b64_tr_b16 v[168:169], v96 offset:0x1c00
	ds_read_b64_tr_b16 v[170:171], v96 offset:0x200
	ds_read_b64_tr_b16 v[172:173], v96 offset:0x600
	ds_read_b64_tr_b16 v[200:201], v96 offset:0xa00
	ds_read_b64_tr_b16 v[202:203], v96 offset:0xe00
	ds_read_b64_tr_b16 v[204:205], v96 offset:0x1200
	ds_read_b64_tr_b16 v[206:207], v96 offset:0x1600
	ds_read_b64_tr_b16 v[208:209], v96 offset:0x1a00
	ds_read_b64_tr_b16 v[210:211], v96 offset:0x1e00
	v_mfma_f32_32x32x16_bf16 v[66:81], v[82:85], v[118:121], v[66:81]
	v_cvt_pk_bf16_f32 v82, v184, v186
	v_cvt_pk_bf16_f32 v83, v185, v187
	v_cvt_pk_bf16_f32 v84, v189, v193
	v_cvt_pk_bf16_f32 v85, v192, v194
	s_nop 0
	v_permlane32_swap_b32_e32 v82, v84
	v_mfma_f32_32x32x16_bf16 v[50:65], v[86:89], v[118:121], v[50:65]
	v_cvt_pk_bf16_f32 v86, v188, v191
	v_cvt_pk_bf16_f32 v87, v190, v196
	v_cvt_pk_bf16_f32 v88, v195, v198
	v_cvt_pk_bf16_f32 v89, v197, v199
	v_cvt_pk_bf16_f32 v122, v34, v35
	v_cvt_pk_bf16_f32 v123, v36, v37
	v_cvt_pk_bf16_f32 v124, v38, v39
	v_cvt_pk_bf16_f32 v125, v40, v41
	v_cvt_pk_bf16_f32 v150, v42, v43
	v_cvt_pk_bf16_f32 v151, v44, v45
	v_cvt_pk_bf16_f32 v152, v46, v47
	v_cvt_pk_bf16_f32 v153, v48, v49
	v_permlane32_swap_b32_e32 v83, v85
	s_waitcnt lgkmcnt(8)
	v_permlane32_swap_b32_e32 v86, v88
	s_nop 0
	v_mfma_f32_32x32x16_bf16 v[2:17], v[82:85], v[154:157], v[2:17]
	s_waitcnt lgkmcnt(0)
	v_permlane32_swap_b32_e32 v87, v89
	v_permlane32_swap_b32_e32 v122, v124
	v_permlane32_swap_b32_e32 v123, v125
	v_mfma_f32_32x32x16_bf16 v[18:33], v[82:85], v[170:173], v[18:33]
	v_permlane32_swap_b32_e32 v150, v152
	v_permlane32_swap_b32_e32 v151, v153
	v_exp_f32_e32 v170, v76
	v_exp_f32_e32 v171, v77
	v_exp_f32_e32 v172, v78
	v_mfma_f32_32x32x16_bf16 v[2:17], v[86:89], v[158:161], v[2:17]
	v_exp_f32_e32 v158, v66
	v_exp_f32_e32 v159, v67
	v_exp_f32_e32 v160, v68
	v_exp_f32_e32 v161, v69
	v_exp_f32_e32 v173, v79
	v_exp_f32_e32 v174, v80
	v_exp_f32_e32 v175, v81
	v_mfma_f32_32x32x16_bf16 v[18:33], v[86:89], v[200:203], v[18:33]
	v_mfma_f32_32x32x16_bf16 v[2:17], v[122:125], v[162:165], v[2:17]
	v_exp_f32_e32 v162, v70
	v_exp_f32_e32 v163, v71
	v_mfma_f32_32x32x16_bf16 v[18:33], v[122:125], v[204:207], v[18:33]
	v_mfma_f32_32x32x16_bf16 v[2:17], v[150:153], v[166:169], v[2:17]
	v_exp_f32_e32 v166, v72
	v_exp_f32_e32 v167, v73
	v_exp_f32_e32 v168, v74
	v_exp_f32_e32 v169, v75
	v_mfma_f32_32x32x16_bf16 v[18:33], v[150:153], v[208:211], v[18:33]

; template <int N> __device__ __forceinline__ void lgkm_wait8(s16x4* v) { asm volatile("s_waitcnt lgkmcnt(%8)" : "+v"(v[0]), "+v"(v[1]), "+v"(v[2]), "+v"(v[3]), "+v"(v[4]), "+v"(v[5]), "+v"(v[6]), "+v"(v[7]) : "n"(N) : "memory"); }
; __device__ __forceinline__ void finishSM(f32x16& p0, f32x16& p1, float& l_reg, bf16x8& pa0, bf16x8& pa1, bf16x8& pa2, bf16x8& pa3) {
; #pragma unroll
;   for (int r = 0; r < 16; ++r) p1[r] = __builtin_amdgcn_exp2f(p1[r]);
;   float ps = 0;
; #pragma unroll
;   for (int r = 0; r < 16; ++r) ps += p0[r];
; #pragma unroll
;   for (int r = 0; r < 16; ++r) ps += p1[r];
;   l_reg += ps;
;     ...
;   ATT_PK4(p0, 0, pa0); ATT_PK4(p0, 8, pa1); ATT_PK4(p1, 0, pa2); ATT_PK4(p1, 8, pa3);
;     ...
; }
; template <int DK>
; __device__ __forceinline__ void qkt(f32x16& p0, f32x16& p1, const char* Ks, const bf16x8* qr, int r32, int hi) {
;   p0 = f32x16{}; p1 = f32x16{};
; #pragma unroll
;   for (int d0 = 0; d0 < DK / 16; ++d0) { const int cb = (d0 * 16 + hi * 8) * 2;
;     const bf16x8 b0 = *reinterpret_cast<const bf16x8*>(Ks + ATT_KSWZ(r32, cb));
;     const bf16x8 b1 = *reinterpret_cast<const bf16x8*>(Ks + ATT_KSWZ(32 + r32, cb));
;     p0 = __builtin_amdgcn_mfma_f32_32x32x16_bf16(b0, qr[d0], p0, 0, 0, 0);
;     p1 = __builtin_amdgcn_mfma_f32_32x32x16_bf16(b1, qr[d0], p1, 0, 0, 0);
;   }
; template <int DV> __device__ __forceinline__ void pv_all_pipe(f32x16* o, int vb, bf16x8 pa0, bf16x8 pa1, bf16x8 pa2, bf16x8 pa3) {
;   s16x4 va[8], vc[8];
;   v_group_read<DV, 0>(va, vb); v_group_read<DV, 1>(vc, vb);
;   lgkm_wait8<8>(va); pv_group(o[0], va, pa0, pa1, pa2, pa3);
;   if constexpr (DV == 128) {
;     s16x4 vd[8], ve[8];
;     v_group_read<DV, 2>(vd, vb);
;     lgkm_wait8<8>(vc); pv_group(o[1], vc, pa0, pa1, pa2, pa3);
;     v_group_read<DV, 3>(ve, vb);
;     lgkm_wait8<8>(vd); pv_group(o[2], vd, pa0, pa1, pa2, pa3);
;     lgkm_wait8<0>(ve); pv_group(o[3], ve, pa0, pa1, pa2, pa3);
;   } else { lgkm_wait8<0>(vc); pv_group(o[1], vc, pa0, pa1, pa2, pa3); }
.Lmstag_1:
	ds_read_b128 v[82:85], v128 offset:49152
	ds_read_b128 v[86:89], v128 offset:57344
	v_add_f32_e32 v0, v167, v0
	v_add_f32_e32 v0, v168, v0
	v_add_f32_e32 v0, v169, v0
	v_add_f32_e32 v0, v170, v0
	v_add_f32_e32 v0, v171, v0
	v_add_f32_e32 v0, v172, v0
	s_waitcnt lgkmcnt(0)
	v_mfma_f32_32x32x16_bf16 v[66:81], v[82:85], v[106:109], v[66:81]
	v_add_f32_e32 v0, v173, v0
	v_add_f32_e32 v0, v174, v0
	v_add_f32_e32 v0, v175, v0
	v_add_f32_e32 v0, v50, v0
	v_add_f32_e32 v0, v51, v0
	v_add_f32_e32 v0, v52, v0
	v_add_f32_e32 v0, v53, v0
	v_mfma_f32_32x32x16_bf16 v[34:49], v[86:89], v[106:109], v[34:49]
	ds_read_b128 v[82:85], v129 offset:49152
	ds_read_b128 v[86:89], v129 offset:57344
	v_add_f32_e32 v0, v54, v0
	v_add_f32_e32 v0, v55, v0
	v_add_f32_e32 v0, v56, v0
	v_add_f32_e32 v0, v57, v0
	v_add_f32_e32 v0, v58, v0
	v_add_f32_e32 v0, v59, v0
	s_waitcnt lgkmcnt(0)
	v_mfma_f32_32x32x16_bf16 v[66:81], v[82:85], v[110:113], v[66:81]
	v_add_f32_e32 v0, v60, v0
	v_add_f32_e32 v0, v61, v0
	v_add_f32_e32 v0, v62, v0
	v_add_f32_e32 v0, v63, v0
	v_add_f32_e32 v0, v64, v0
	v_add_f32_e32 v0, v65, v0
	v_add_f32_e32 v145, v145, v0
	v_mfma_f32_32x32x16_bf16 v[34:49], v[86:89], v[110:113], v[34:49]
	ds_read_b128 v[82:85], v130 offset:49152
	ds_read_b128 v[86:89], v130 offset:57344
	s_andn2_b64 vcc, exec, s[38:39]
	s_waitcnt lgkmcnt(0)
	v_mfma_f32_32x32x16_bf16 v[66:81], v[82:85], v[114:117], v[66:81]
	v_mfma_f32_32x32x16_bf16 v[34:49], v[86:89], v[114:117], v[34:49]
	ds_read_b128 v[82:85], v131 offset:49152
	ds_read_b128 v[86:89], v131 offset:57344
	s_waitcnt lgkmcnt(0)
	ds_read_b64_tr_b16 v[154:155], v132 offset:0
	ds_read_b64_tr_b16 v[156:157], v132 offset:0x400
	ds_read_b64_tr_b16 v[184:185], v132 offset:0x800
	ds_read_b64_tr_b16 v[186:187], v132 offset:0xc00
	ds_read_b64_tr_b16 v[188:189], v132 offset:0x1000
	ds_read_b64_tr_b16 v[190:191], v132 offset:0x1400
	ds_read_b64_tr_b16 v[192:193], v132 offset:0x1800
	ds_read_b64_tr_b16 v[194:195], v132 offset:0x1c00
	ds_read_b64_tr_b16 v[196:197], v132 offset:0x200
	ds_read_b64_tr_b16 v[198:199], v132 offset:0x600
	ds_read_b64_tr_b16 v[200:201], v132 offset:0xa00
	ds_read_b64_tr_b16 v[202:203], v132 offset:0xe00
	ds_read_b64_tr_b16 v[204:205], v132 offset:0x1200
	ds_read_b64_tr_b16 v[206:207], v132 offset:0x1600
	ds_read_b64_tr_b16 v[208:209], v132 offset:0x1a00
	ds_read_b64_tr_b16 v[210:211], v132 offset:0x1e00
	v_mfma_f32_32x32x16_bf16 v[66:81], v[82:85], v[118:121], v[66:81]
	v_cvt_pk_bf16_f32 v82, v158, v159
	v_cvt_pk_bf16_f32 v83, v160, v161
	v_cvt_pk_bf16_f32 v84, v162, v163
	v_cvt_pk_bf16_f32 v85, v166, v167
	s_nop 0
	v_permlane32_swap_b32_e32 v82, v84
	v_mfma_f32_32x32x16_bf16 v[34:49], v[86:89], v[118:121], v[34:49]
	v_cvt_pk_bf16_f32 v86, v168, v169
	v_cvt_pk_bf16_f32 v87, v170, v171
	v_cvt_pk_bf16_f32 v88, v172, v173
	v_cvt_pk_bf16_f32 v89, v174, v175
	v_cvt_pk_bf16_f32 v122, v50, v51
	v_cvt_pk_bf16_f32 v123, v52, v53
	v_cvt_pk_bf16_f32 v124, v54, v55
	v_cvt_pk_bf16_f32 v125, v56, v57
	v_cvt_pk_bf16_f32 v150, v58, v59
	v_cvt_pk_bf16_f32 v151, v60, v61
	v_cvt_pk_bf16_f32 v152, v62, v63
	v_cvt_pk_bf16_f32 v153, v64, v65
	v_permlane32_swap_b32_e32 v83, v85
	s_waitcnt lgkmcnt(8)
	v_permlane32_swap_b32_e32 v86, v88
	s_nop 0
	v_mfma_f32_32x32x16_bf16 v[2:17], v[82:85], v[154:157], v[2:17]
	s_waitcnt lgkmcnt(0)
	v_permlane32_swap_b32_e32 v87, v89
	v_permlane32_swap_b32_e32 v122, v124
	v_permlane32_swap_b32_e32 v123, v125
	v_mfma_f32_32x32x16_bf16 v[18:33], v[82:85], v[196:199], v[18:33]
	v_permlane32_swap_b32_e32 v150, v152
	v_permlane32_swap_b32_e32 v151, v153
	v_exp_f32_e32 v196, v77
	v_exp_f32_e32 v198, v79
	v_exp_f32_e32 v197, v80
	v_mfma_f32_32x32x16_bf16 v[2:17], v[86:89], v[184:187], v[2:17]
	v_exp_f32_e32 v184, v66
	v_exp_f32_e32 v186, v67
	v_exp_f32_e32 v185, v68
	v_exp_f32_e32 v187, v69
	v_exp_f32_e32 v199, v81
	v_mfma_f32_32x32x16_bf16 v[18:33], v[86:89], v[200:203], v[18:33]
	v_mfma_f32_32x32x16_bf16 v[2:17], v[122:125], v[188:191], v[2:17]
	v_exp_f32_e32 v189, v70
	v_exp_f32_e32 v188, v74
	v_exp_f32_e32 v191, v75
	v_exp_f32_e32 v190, v76
	v_mfma_f32_32x32x16_bf16 v[18:33], v[122:125], v[204:207], v[18:33]
	v_mfma_f32_32x32x16_bf16 v[2:17], v[150:153], v[192:195], v[2:17]
	v_exp_f32_e32 v193, v71
	v_exp_f32_e32 v192, v72
	v_exp_f32_e32 v194, v73
	v_exp_f32_e32 v195, v78
	v_mfma_f32_32x32x16_bf16 v[18:33], v[150:153], v[208:211], v[18:33]
	s_cbranch_vccnz .LBB0_1449

; template <int N> __device__ __forceinline__ void lgkm_wait8(s16x4* v) { asm volatile("s_waitcnt lgkmcnt(%8)" : "+v"(v[0]), "+v"(v[1]), "+v"(v[2]), "+v"(v[3]), "+v"(v[4]), "+v"(v[5]), "+v"(v[6]), "+v"(v[7]) : "n"(N) : "memory"); }
; __device__ __forceinline__ void finishSM(f32x16& p0, f32x16& p1, float& l_reg, bf16x8& pa0, bf16x8& pa1, bf16x8& pa2, bf16x8& pa3) {
; #pragma unroll
;   for (int r = 0; r < 16; ++r) p1[r] = __builtin_amdgcn_exp2f(p1[r]);
;   float ps = 0;
; #pragma unroll
;   for (int r = 0; r < 16; ++r) ps += p0[r];
; #pragma unroll
;   for (int r = 0; r < 16; ++r) ps += p1[r];
;   l_reg += ps;
;     ...
;   ATT_PK4(p0, 0, pa0); ATT_PK4(p0, 8, pa1); ATT_PK4(p1, 0, pa2); ATT_PK4(p1, 8, pa3);
;     ...
; }
; template <int DK>
; __device__ __forceinline__ void qkt(f32x16& p0, f32x16& p1, const char* Ks, const bf16x8* qr, int r32, int hi) {
;   p0 = f32x16{}; p1 = f32x16{};
; #pragma unroll
;   for (int d0 = 0; d0 < DK / 16; ++d0) { const int cb = (d0 * 16 + hi * 8) * 2;
;     const bf16x8 b0 = *reinterpret_cast<const bf16x8*>(Ks + ATT_KSWZ(r32, cb));
;     const bf16x8 b1 = *reinterpret_cast<const bf16x8*>(Ks + ATT_KSWZ(32 + r32, cb));
;     p0 = __builtin_amdgcn_mfma_f32_32x32x16_bf16(b0, qr[d0], p0, 0, 0, 0);
;     p1 = __builtin_amdgcn_mfma_f32_32x32x16_bf16(b1, qr[d0], p1, 0, 0, 0);
;   }
; template <int DV> __device__ __forceinline__ void pv_all_pipe(f32x16* o, int vb, bf16x8 pa0, bf16x8 pa1, bf16x8 pa2, bf16x8 pa3) {
;   s16x4 va[8], vc[8];
;   v_group_read<DV, 0>(va, vb); v_group_read<DV, 1>(vc, vb);
;   lgkm_wait8<8>(va); pv_group(o[0], va, pa0, pa1, pa2, pa3);
;   if constexpr (DV == 128) {
;     s16x4 vd[8], ve[8];
;     v_group_read<DV, 2>(vd, vb);
;     lgkm_wait8<8>(vc); pv_group(o[1], vc, pa0, pa1, pa2, pa3);
;     v_group_read<DV, 3>(ve, vb);
;     lgkm_wait8<8>(vd); pv_group(o[2], vd, pa0, pa1, pa2, pa3);
;     lgkm_wait8<0>(ve); pv_group(o[3], ve, pa0, pa1, pa2, pa3);
;   } else { lgkm_wait8<0>(vc); pv_group(o[1], vc, pa0, pa1, pa2, pa3); }
.Lmstag_2:
	ds_read_b128 v[82:85], v135
	ds_read_b128 v[86:89], v135 offset:8192
	v_add_f32_e32 v0, v194, v0
	v_add_f32_e32 v0, v188, v0
	v_add_f32_e32 v0, v191, v0
	v_add_f32_e32 v0, v190, v0
	v_add_f32_e32 v0, v196, v0
	v_add_f32_e32 v0, v195, v0
	s_waitcnt lgkmcnt(0)
	v_mfma_f32_32x32x16_bf16 v[66:81], v[82:85], v[106:109], v[66:81]
	v_add_f32_e32 v0, v198, v0
	v_add_f32_e32 v0, v197, v0
	v_add_f32_e32 v0, v199, v0
	v_add_f32_e32 v0, v34, v0
	v_add_f32_e32 v0, v35, v0
	v_add_f32_e32 v0, v36, v0
	v_add_f32_e32 v0, v37, v0
	v_mfma_f32_32x32x16_bf16 v[50:65], v[86:89], v[106:109], v[50:65]
	ds_read_b128 v[82:85], v136
	ds_read_b128 v[86:89], v136 offset:8192
	v_add_f32_e32 v0, v38, v0
	v_add_f32_e32 v0, v39, v0
	v_add_f32_e32 v0, v40, v0
	v_add_f32_e32 v0, v41, v0
	v_add_f32_e32 v0, v42, v0
	v_add_f32_e32 v0, v43, v0
	s_waitcnt lgkmcnt(0)
	v_mfma_f32_32x32x16_bf16 v[66:81], v[82:85], v[110:113], v[66:81]
	v_add_f32_e32 v0, v44, v0
	v_add_f32_e32 v0, v45, v0
	v_add_f32_e32 v0, v46, v0
	v_add_f32_e32 v0, v47, v0
	v_add_f32_e32 v0, v48, v0
	v_add_f32_e32 v0, v49, v0
	v_add_f32_e32 v145, v145, v0
	v_mfma_f32_32x32x16_bf16 v[50:65], v[86:89], v[110:113], v[50:65]
	ds_read_b128 v[82:85], v137
	ds_read_b128 v[86:89], v137 offset:8192
	s_waitcnt lgkmcnt(0)
	v_mfma_f32_32x32x16_bf16 v[66:81], v[82:85], v[114:117], v[66:81]
	v_mfma_f32_32x32x16_bf16 v[50:65], v[86:89], v[114:117], v[50:65]
	ds_read_b128 v[82:85], v138
	ds_read_b128 v[86:89], v138 offset:8192
	s_waitcnt lgkmcnt(0)
	ds_read_b64_tr_b16 v[154:155], v139 offset:0
	ds_read_b64_tr_b16 v[156:157], v139 offset:0x400
	ds_read_b64_tr_b16 v[158:159], v139 offset:0x800
	ds_read_b64_tr_b16 v[160:161], v139 offset:0xc00
	ds_read_b64_tr_b16 v[162:163], v139 offset:0x1000
	ds_read_b64_tr_b16 v[164:165], v139 offset:0x1400
	ds_read_b64_tr_b16 v[166:167], v139 offset:0x1800
	ds_read_b64_tr_b16 v[168:169], v139 offset:0x1c00
	ds_read_b64_tr_b16 v[170:171], v139 offset:0x200
	ds_read_b64_tr_b16 v[172:173], v139 offset:0x600
	ds_read_b64_tr_b16 v[200:201], v139 offset:0xa00
	ds_read_b64_tr_b16 v[202:203], v139 offset:0xe00
	ds_read_b64_tr_b16 v[204:205], v139 offset:0x1200
	ds_read_b64_tr_b16 v[206:207], v139 offset:0x1600
	ds_read_b64_tr_b16 v[208:209], v139 offset:0x1a00
	ds_read_b64_tr_b16 v[210:211], v139 offset:0x1e00
	v_mfma_f32_32x32x16_bf16 v[66:81], v[82:85], v[118:121], v[66:81]
	v_cvt_pk_bf16_f32 v82, v184, v186
	v_cvt_pk_bf16_f32 v83, v185, v187
	v_cvt_pk_bf16_f32 v84, v189, v193
	v_cvt_pk_bf16_f32 v85, v192, v194
	s_nop 0
	v_permlane32_swap_b32_e32 v82, v84
	v_mfma_f32_32x32x16_bf16 v[50:65], v[86:89], v[118:121], v[50:65]
	v_cvt_pk_bf16_f32 v86, v188, v191
	v_cvt_pk_bf16_f32 v87, v190, v196
	v_cvt_pk_bf16_f32 v88, v195, v198
	v_cvt_pk_bf16_f32 v89, v197, v199
	v_cvt_pk_bf16_f32 v122, v34, v35
	v_cvt_pk_bf16_f32 v123, v36, v37
	v_cvt_pk_bf16_f32 v124, v38, v39
	v_cvt_pk_bf16_f32 v125, v40, v41
	v_cvt_pk_bf16_f32 v150, v42, v43
	v_cvt_pk_bf16_f32 v151, v44, v45
	v_cvt_pk_bf16_f32 v152, v46, v47
	v_cvt_pk_bf16_f32 v153, v48, v49
	v_permlane32_swap_b32_e32 v83, v85
	s_waitcnt lgkmcnt(8)
	v_permlane32_swap_b32_e32 v86, v88
	s_nop 0
	v_mfma_f32_32x32x16_bf16 v[2:17], v[82:85], v[154:157], v[2:17]
	s_waitcnt lgkmcnt(0)
	v_permlane32_swap_b32_e32 v87, v89
	v_permlane32_swap_b32_e32 v122, v124
	v_permlane32_swap_b32_e32 v123, v125
	v_mfma_f32_32x32x16_bf16 v[18:33], v[82:85], v[170:173], v[18:33]
	v_permlane32_swap_b32_e32 v150, v152
	v_permlane32_swap_b32_e32 v151, v153
	v_exp_f32_e32 v170, v76
	v_exp_f32_e32 v171, v77
	v_exp_f32_e32 v172, v78
	v_mfma_f32_32x32x16_bf16 v[2:17], v[86:89], v[158:161], v[2:17]
	v_exp_f32_e32 v158, v66
	v_exp_f32_e32 v159, v67
	v_exp_f32_e32 v160, v68
	v_exp_f32_e32 v161, v69
	v_exp_f32_e32 v173, v79
	v_exp_f32_e32 v174, v80
	v_exp_f32_e32 v175, v81
	v_mfma_f32_32x32x16_bf16 v[18:33], v[86:89], v[200:203], v[18:33]
	v_mfma_f32_32x32x16_bf16 v[2:17], v[122:125], v[162:165], v[2:17]
	v_exp_f32_e32 v162, v70
	v_exp_f32_e32 v163, v71
	v_mfma_f32_32x32x16_bf16 v[18:33], v[122:125], v[204:207], v[18:33]
	v_mfma_f32_32x32x16_bf16 v[2:17], v[150:153], v[166:169], v[2:17]
	v_exp_f32_e32 v166, v72
	v_exp_f32_e32 v167, v73
	v_exp_f32_e32 v168, v74
	v_exp_f32_e32 v169, v75
	v_mfma_f32_32x32x16_bf16 v[18:33], v[150:153], v[208:211], v[18:33]
	s_andn2_b64 vcc, exec, s[0:1]
	s_cbranch_vccz .LBB0_1450

; template <int N> __device__ __forceinline__ void lgkm_wait8(s16x4* v) { asm volatile("s_waitcnt lgkmcnt(%8)" : "+v"(v[0]), "+v"(v[1]), "+v"(v[2]), "+v"(v[3]), "+v"(v[4]), "+v"(v[5]), "+v"(v[6]), "+v"(v[7]) : "n"(N) : "memory"); }
; __device__ __forceinline__ void finishSM(f32x16& p0, f32x16& p1, float& l_reg, bf16x8& pa0, bf16x8& pa1, bf16x8& pa2, bf16x8& pa3) {
; #pragma unroll
;   for (int r = 0; r < 16; ++r) p1[r] = __builtin_amdgcn_exp2f(p1[r]);
;   float ps = 0;
; #pragma unroll
;   for (int r = 0; r < 16; ++r) ps += p0[r];
; #pragma unroll
;   for (int r = 0; r < 16; ++r) ps += p1[r];
;   l_reg += ps;
;     ...
;   ATT_PK4(p0, 0, pa0); ATT_PK4(p0, 8, pa1); ATT_PK4(p1, 0, pa2); ATT_PK4(p1, 8, pa3);
;     ...
; }
; template <int DK>
; __device__ __forceinline__ void qkt(f32x16& p0, f32x16& p1, const char* Ks, const bf16x8* qr, int r32, int hi) {
;   p0 = f32x16{}; p1 = f32x16{};
; #pragma unroll
;   for (int d0 = 0; d0 < DK / 16; ++d0) { const int cb = (d0 * 16 + hi * 8) * 2;
;     const bf16x8 b0 = *reinterpret_cast<const bf16x8*>(Ks + ATT_KSWZ(r32, cb));
;     const bf16x8 b1 = *reinterpret_cast<const bf16x8*>(Ks + ATT_KSWZ(32 + r32, cb));
;     p0 = __builtin_amdgcn_mfma_f32_32x32x16_bf16(b0, qr[d0], p0, 0, 0, 0);
;     p1 = __builtin_amdgcn_mfma_f32_32x32x16_bf16(b1, qr[d0], p1, 0, 0, 0);
;   }
; template <int DV> __device__ __forceinline__ void pv_all_pipe(f32x16* o, int vb, bf16x8 pa0, bf16x8 pa1, bf16x8 pa2, bf16x8 pa3) {
;   s16x4 va[8], vc[8];
;   v_group_read<DV, 0>(va, vb); v_group_read<DV, 1>(vc, vb);
;   lgkm_wait8<8>(va); pv_group(o[0], va, pa0, pa1, pa2, pa3);
;   if constexpr (DV == 128) {
;     s16x4 vd[8], ve[8];
;     v_group_read<DV, 2>(vd, vb);
;     lgkm_wait8<8>(vc); pv_group(o[1], vc, pa0, pa1, pa2, pa3);
;     v_group_read<DV, 3>(ve, vb);
;     lgkm_wait8<8>(vd); pv_group(o[2], vd, pa0, pa1, pa2, pa3);
;     lgkm_wait8<0>(ve); pv_group(o[3], ve, pa0, pa1, pa2, pa3);
;   } else { lgkm_wait8<0>(vc); pv_group(o[1], vc, pa0, pa1, pa2, pa3); }
.Lmstag_3:
	ds_read_b128 v[82:85], v142
	ds_read_b128 v[86:89], v142 offset:8192
	v_add_f32_e32 v0, v167, v0
	v_add_f32_e32 v0, v168, v0
	v_add_f32_e32 v0, v169, v0
	v_add_f32_e32 v0, v170, v0
	v_add_f32_e32 v0, v171, v0
	v_add_f32_e32 v0, v172, v0
	s_waitcnt lgkmcnt(0)
	v_mfma_f32_32x32x16_bf16 v[66:81], v[82:85], v[106:109], v[66:81]
	v_add_f32_e32 v0, v173, v0
	v_add_f32_e32 v0, v174, v0
	v_add_f32_e32 v0, v175, v0
	v_add_f32_e32 v0, v50, v0
	v_add_f32_e32 v0, v51, v0
	v_add_f32_e32 v0, v52, v0
	v_add_f32_e32 v0, v53, v0
	v_mfma_f32_32x32x16_bf16 v[34:49], v[86:89], v[106:109], v[34:49]
	ds_read_b128 v[82:85], v143
	ds_read_b128 v[86:89], v143 offset:8192
	v_add_f32_e32 v0, v54, v0
	v_add_f32_e32 v0, v55, v0
	v_add_f32_e32 v0, v56, v0
	v_add_f32_e32 v0, v57, v0
	v_add_f32_e32 v0, v58, v0
	v_add_f32_e32 v0, v59, v0
	s_waitcnt lgkmcnt(0)
	v_mfma_f32_32x32x16_bf16 v[66:81], v[82:85], v[110:113], v[66:81]
	v_add_f32_e32 v0, v60, v0
	v_add_f32_e32 v0, v61, v0
	v_add_f32_e32 v0, v62, v0
	v_add_f32_e32 v0, v63, v0
	v_add_f32_e32 v0, v64, v0
	v_add_f32_e32 v0, v65, v0
	v_add_f32_e32 v145, v145, v0
	v_mfma_f32_32x32x16_bf16 v[34:49], v[86:89], v[110:113], v[34:49]
	ds_read_b128 v[82:85], v144
	ds_read_b128 v[86:89], v144 offset:8192
	s_waitcnt lgkmcnt(0)
	v_mfma_f32_32x32x16_bf16 v[66:81], v[82:85], v[114:117], v[66:81]
	v_mfma_f32_32x32x16_bf16 v[34:49], v[86:89], v[114:117], v[34:49]
	ds_read_b128 v[82:85], v148
	ds_read_b128 v[86:89], v148 offset:8192
	s_waitcnt lgkmcnt(0)
	ds_read_b64_tr_b16 v[154:155], v97 offset:0
	ds_read_b64_tr_b16 v[156:157], v97 offset:0x400
	ds_read_b64_tr_b16 v[184:185], v97 offset:0x800
	ds_read_b64_tr_b16 v[186:187], v97 offset:0xc00
	ds_read_b64_tr_b16 v[188:189], v97 offset:0x1000
	ds_read_b64_tr_b16 v[190:191], v97 offset:0x1400
	ds_read_b64_tr_b16 v[192:193], v97 offset:0x1800
	ds_read_b64_tr_b16 v[194:195], v97 offset:0x1c00
	ds_read_b64_tr_b16 v[196:197], v97 offset:0x200
	ds_read_b64_tr_b16 v[198:199], v97 offset:0x600
	ds_read_b64_tr_b16 v[200:201], v97 offset:0xa00
	ds_read_b64_tr_b16 v[202:203], v97 offset:0xe00
	ds_read_b64_tr_b16 v[204:205], v97 offset:0x1200
	ds_read_b64_tr_b16 v[206:207], v97 offset:0x1600
	ds_read_b64_tr_b16 v[208:209], v97 offset:0x1a00
	ds_read_b64_tr_b16 v[210:211], v97 offset:0x1e00
	v_mfma_f32_32x32x16_bf16 v[66:81], v[82:85], v[118:121], v[66:81]
	v_cvt_pk_bf16_f32 v82, v158, v159
	v_cvt_pk_bf16_f32 v83, v160, v161
	v_cvt_pk_bf16_f32 v84, v162, v163
	v_cvt_pk_bf16_f32 v85, v166, v167
	s_nop 0
	v_permlane32_swap_b32_e32 v82, v84
	v_mfma_f32_32x32x16_bf16 v[34:49], v[86:89], v[118:121], v[34:49]
	v_cvt_pk_bf16_f32 v86, v168, v169
	v_cvt_pk_bf16_f32 v87, v170, v171
	v_cvt_pk_bf16_f32 v88, v172, v173
	v_cvt_pk_bf16_f32 v89, v174, v175
	v_cvt_pk_bf16_f32 v122, v50, v51
	v_cvt_pk_bf16_f32 v123, v52, v53
	v_cvt_pk_bf16_f32 v124, v54, v55
	v_cvt_pk_bf16_f32 v125, v56, v57
	v_cvt_pk_bf16_f32 v150, v58, v59
	v_cvt_pk_bf16_f32 v151, v60, v61
	v_cvt_pk_bf16_f32 v152, v62, v63
	v_cvt_pk_bf16_f32 v153, v64, v65
	v_permlane32_swap_b32_e32 v83, v85
	s_waitcnt lgkmcnt(8)
	v_permlane32_swap_b32_e32 v86, v88
	s_nop 0
	v_mfma_f32_32x32x16_bf16 v[2:17], v[82:85], v[154:157], v[2:17]
	s_waitcnt lgkmcnt(0)
	v_permlane32_swap_b32_e32 v87, v89
	v_permlane32_swap_b32_e32 v122, v124
	v_permlane32_swap_b32_e32 v123, v125
	v_mfma_f32_32x32x16_bf16 v[18:33], v[82:85], v[196:199], v[18:33]
	v_permlane32_swap_b32_e32 v150, v152
	v_permlane32_swap_b32_e32 v151, v153
	v_exp_f32_e32 v196, v77
	v_exp_f32_e32 v198, v79
	v_exp_f32_e32 v197, v80
	v_mfma_f32_32x32x16_bf16 v[2:17], v[86:89], v[184:187], v[2:17]
	v_exp_f32_e32 v184, v66
	v_exp_f32_e32 v186, v67
	v_exp_f32_e32 v185, v68
	v_exp_f32_e32 v187, v69
	v_exp_f32_e32 v199, v81
	v_mfma_f32_32x32x16_bf16 v[18:33], v[86:89], v[200:203], v[18:33]
	v_mfma_f32_32x32x16_bf16 v[2:17], v[122:125], v[188:191], v[2:17]
	v_exp_f32_e32 v189, v70
	v_exp_f32_e32 v188, v74
	v_exp_f32_e32 v191, v75
	v_exp_f32_e32 v190, v76
	v_mfma_f32_32x32x16_bf16 v[18:33], v[122:125], v[204:207], v[18:33]
	v_mfma_f32_32x32x16_bf16 v[2:17], v[150:153], v[192:195], v[2:17]
	v_exp_f32_e32 v193, v71
	v_exp_f32_e32 v192, v72
	v_exp_f32_e32 v194, v73
	v_exp_f32_e32 v195, v78
	v_mfma_f32_32x32x16_bf16 v[18:33], v[150:153], v[208:211], v[18:33]
	s_cmp_ge_u32 s92, s90
	s_cbranch_scc1 .LBB0_1433
